# P1 head-norm: precise 1/sqrtf chains replaced by v_rsq_f32 (f32)
# baseline (speedup 1.0000x reference)
; #define LAS __attribute__((address_space(3)))
; #define EPI_BAR() do { asm volatile("s_waitcnt lgkmcnt(0)" ::: "memory"); __builtin_amdgcn_s_barrier(); asm volatile("" ::: "memory"); } while (0)
;     __device__ __forceinline__ void operator()(Acc& acc, const Unit& u, int wr, int wc, int fr, int fq, LAS unsigned char* le, int wid, int lane, int& cpm) const {
;     ...
;             EPI_BAR();
;             const float* gn = gains + ((type == 0) ? 0 : (type == 1) ? 128 : (type == 3) ? 256 : 384) + wc * 32 + fq * 8;
;             const f32x4 g0 = *(const f32x4*)gn, g1 = *(const f32x4*)(gn + 4);
; #pragma unroll
;             for (int ai = 0; ai < 2; ++ai)
; #pragma unroll
;                 for (int m = 0; m < 4; ++m)
; #pragma unroll
;                     for (int bj = 0; bj < 2; ++bj) {
;                         const f32x4 pp = *(const LAS f32x4*)(P + ((ai * 128 + wr * 64 + m * 16 + fr) * 2 + bj) * 4);
;                         const float rn = 1.0f / sqrtf(((pp[0] + pp[1]) + (pp[2] + pp[3])) * (1.0f / HD) + EPS);
;                         acc[ai][bj][m][0] = acc[ai][bj][m][0] * rn * g0; acc[ai][bj][m][1] = acc[ai][bj][m][1] * rn * g1;
;                     }
.LBB0_306:
	s_or_b64 exec, exec, s[14:15]
	s_cmp_eq_u32 s3, 3
	s_movk_i32 s14, 0x180
	s_cselect_b32 s14, 0x100, s14
	s_cmp_lg_u32 s3, 1
	s_cselect_b32 s14, s14, 0x80
	s_cmp_gt_u32 s24, 3
	s_cselect_b32 s14, s14, 0
	s_lshl_b32 s16, s14, 2
	s_waitcnt lgkmcnt(0)
	s_barrier
	v_lshl_add_u64 v[132:133], v[162:163], 0, s[16:17]
	v_add_u32_e32 v140, s61, v199
	s_waitcnt lgkmcnt(0)
	global_load_dwordx4 v[128:131], v[132:133], off offset:16
	s_nop 0
	global_load_dwordx4 v[132:135], v[132:133], off
	ds_read_b128 v[136:139], v140
	ds_read_b128 v[140:143], v140 offset:16
	s_cmp_lt_i32 s3, 3
	s_waitcnt lgkmcnt(0)
	v_mov_b32_e32 v174, v137
	v_mov_b32_e32 v175, v138
	v_mov_b32_e32 v137, v139
	v_pk_add_f32 v[136:137], v[174:175], v[136:137]
	s_nop 0
	v_add_f32_e32 v136, v136, v137
	v_fmamk_f32 v136, v136, 0x3c000000, v205
	v_rsq_f32_e32 v136, v136
	s_nop 0
	v_pk_mul_f32 v[80:81], v[80:81], v[136:137] op_sel_hi:[1,0]
	v_pk_mul_f32 v[82:83], v[82:83], v[136:137] op_sel_hi:[1,0]
	v_pk_mul_f32 v[92:93], v[92:93], v[136:137] op_sel_hi:[1,0]
	v_pk_mul_f32 v[94:95], v[94:95], v[136:137] op_sel_hi:[1,0]
	v_mov_b32_e32 v136, v141
	v_mov_b32_e32 v137, v142
	v_mov_b32_e32 v141, v143
	v_pk_add_f32 v[136:137], v[136:137], v[140:141]
	s_waitcnt vmcnt(0)
	v_pk_mul_f32 v[94:95], v[130:131], v[94:95]
	v_add_f32_e32 v136, v136, v137
	v_fmamk_f32 v136, v136, 0x3c000000, v205
	v_pk_mul_f32 v[82:83], v[134:135], v[82:83]
	v_pk_mul_f32 v[80:81], v[132:133], v[80:81]
	v_pk_mul_f32 v[92:93], v[128:129], v[92:93]
	v_rsq_f32_e32 v136, v136
	s_nop 0
	v_add_u32_e32 v140, s63, v199
	v_pk_mul_f32 v[120:121], v[120:121], v[136:137] op_sel_hi:[1,0]
	v_pk_mul_f32 v[122:123], v[122:123], v[136:137] op_sel_hi:[1,0]
	v_pk_mul_f32 v[124:125], v[124:125], v[136:137] op_sel_hi:[1,0]
	v_pk_mul_f32 v[126:127], v[126:127], v[136:137] op_sel_hi:[1,0]
	ds_read_b128 v[136:139], v140
	ds_read_b128 v[140:143], v140 offset:16
	v_pk_mul_f32 v[122:123], v[134:135], v[122:123]
	v_pk_mul_f32 v[120:121], v[132:133], v[120:121]
	v_pk_mul_f32 v[126:127], v[130:131], v[126:127]
	s_waitcnt lgkmcnt(1)
	v_mov_b32_e32 v174, v137
	v_mov_b32_e32 v175, v138
	v_mov_b32_e32 v137, v139
	v_pk_add_f32 v[136:137], v[174:175], v[136:137]
	v_pk_mul_f32 v[124:125], v[128:129], v[124:125]
	v_add_f32_e32 v136, v136, v137
	v_fmamk_f32 v136, v136, 0x3c000000, v205
	v_rsq_f32_e32 v136, v136
	s_nop 0
	v_pk_mul_f32 v[52:53], v[52:53], v[136:137] op_sel_hi:[1,0]
	v_pk_mul_f32 v[54:55], v[54:55], v[136:137] op_sel_hi:[1,0]
	v_pk_mul_f32 v[68:69], v[68:69], v[136:137] op_sel_hi:[1,0]
	v_pk_mul_f32 v[70:71], v[70:71], v[136:137] op_sel_hi:[1,0]
	s_waitcnt lgkmcnt(0)
	v_mov_b32_e32 v136, v141
	v_mov_b32_e32 v137, v142
	v_mov_b32_e32 v141, v143
	v_pk_add_f32 v[136:137], v[136:137], v[140:141]
	v_pk_mul_f32 v[54:55], v[134:135], v[54:55]
	v_add_f32_e32 v136, v136, v137
	v_fmamk_f32 v136, v136, 0x3c000000, v205
	v_pk_mul_f32 v[52:53], v[132:133], v[52:53]
	v_pk_mul_f32 v[70:71], v[130:131], v[70:71]
	v_pk_mul_f32 v[68:69], v[128:129], v[68:69]
	v_rsq_f32_e32 v136, v136
	s_nop 0
	v_add_u32_e32 v140, s64, v199
	v_pk_mul_f32 v[104:105], v[104:105], v[136:137] op_sel_hi:[1,0]
	v_pk_mul_f32 v[106:107], v[106:107], v[136:137] op_sel_hi:[1,0]
	v_pk_mul_f32 v[112:113], v[112:113], v[136:137] op_sel_hi:[1,0]
	v_pk_mul_f32 v[114:115], v[114:115], v[136:137] op_sel_hi:[1,0]
	ds_read_b128 v[136:139], v140
	ds_read_b128 v[140:143], v140 offset:16
	v_pk_mul_f32 v[106:107], v[134:135], v[106:107]
	v_pk_mul_f32 v[104:105], v[132:133], v[104:105]
	v_pk_mul_f32 v[114:115], v[130:131], v[114:115]
	s_waitcnt lgkmcnt(1)
	v_mov_b32_e32 v174, v137
	v_mov_b32_e32 v175, v138
	v_mov_b32_e32 v137, v139
	v_pk_add_f32 v[136:137], v[174:175], v[136:137]
	v_pk_mul_f32 v[112:113], v[128:129], v[112:113]
	v_add_f32_e32 v136, v136, v137
	v_fmamk_f32 v136, v136, 0x3c000000, v205
	v_rsq_f32_e32 v136, v136
	s_nop 0
	v_pk_mul_f32 v[28:29], v[28:29], v[136:137] op_sel_hi:[1,0]
	v_pk_mul_f32 v[30:31], v[30:31], v[136:137] op_sel_hi:[1,0]
	v_pk_mul_f32 v[36:37], v[36:37], v[136:137] op_sel_hi:[1,0]
	v_pk_mul_f32 v[38:39], v[38:39], v[136:137] op_sel_hi:[1,0]
	s_waitcnt lgkmcnt(0)
	v_mov_b32_e32 v136, v141
	v_mov_b32_e32 v137, v142
	v_mov_b32_e32 v141, v143
	v_pk_add_f32 v[136:137], v[136:137], v[140:141]
	v_pk_mul_f32 v[30:31], v[134:135], v[30:31]
	v_add_f32_e32 v136, v136, v137
	v_fmamk_f32 v136, v136, 0x3c000000, v205
	v_pk_mul_f32 v[28:29], v[132:133], v[28:29]
	v_pk_mul_f32 v[38:39], v[130:131], v[38:39]
	v_pk_mul_f32 v[36:37], v[128:129], v[36:37]
	v_rsq_f32_e32 v136, v136
	s_nop 0
	v_add_u32_e32 v140, s65, v199
	v_pk_mul_f32 v[84:85], v[84:85], v[136:137] op_sel_hi:[1,0]
	v_pk_mul_f32 v[86:87], v[86:87], v[136:137] op_sel_hi:[1,0]
	v_pk_mul_f32 v[96:97], v[96:97], v[136:137] op_sel_hi:[1,0]
	v_pk_mul_f32 v[98:99], v[98:99], v[136:137] op_sel_hi:[1,0]
	ds_read_b128 v[136:139], v140
	ds_read_b128 v[140:143], v140 offset:16
	v_pk_mul_f32 v[86:87], v[134:135], v[86:87]
	v_pk_mul_f32 v[84:85], v[132:133], v[84:85]
	v_pk_mul_f32 v[98:99], v[130:131], v[98:99]
	s_waitcnt lgkmcnt(1)
	v_mov_b32_e32 v174, v137
	v_mov_b32_e32 v175, v138
	v_mov_b32_e32 v137, v139
	v_pk_add_f32 v[136:137], v[174:175], v[136:137]
	v_pk_mul_f32 v[96:97], v[128:129], v[96:97]
	v_add_f32_e32 v136, v136, v137
	v_fmamk_f32 v136, v136, 0x3c000000, v205
	v_rsq_f32_e32 v136, v136
	s_nop 0
	v_pk_mul_f32 v[8:9], v[8:9], v[136:137] op_sel_hi:[1,0]
	v_pk_mul_f32 v[10:11], v[10:11], v[136:137] op_sel_hi:[1,0]
	v_pk_mul_f32 v[16:17], v[16:17], v[136:137] op_sel_hi:[1,0]
	v_pk_mul_f32 v[18:19], v[18:19], v[136:137] op_sel_hi:[1,0]
	s_waitcnt lgkmcnt(0)
; #define LAS __attribute__((address_space(3)))
;     __device__ __forceinline__ void operator()(Acc& acc, const Unit& u, int wr, int wc, int fr, int fq, LAS unsigned char* le, int wid, int lane, int& cpm) const {
;     ...
;             for (int ai = 0; ai < 2; ++ai)
; #pragma unroll
;                 for (int m = 0; m < 4; ++m)
; #pragma unroll
;                     for (int bj = 0; bj < 2; ++bj) {
;                         const f32x4 pp = *(const LAS f32x4*)(P + ((ai * 128 + wr * 64 + m * 16 + fr) * 2 + bj) * 4);
;                         const float rn = 1.0f / sqrtf(((pp[0] + pp[1]) + (pp[2] + pp[3])) * (1.0f / HD) + EPS);
;                         acc[ai][bj][m][0] = acc[ai][bj][m][0] * rn * g0; acc[ai][bj][m][1] = acc[ai][bj][m][1] * rn * g1;
;                     }
;             if (type >= 3 && wc == 0) {
	v_mov_b32_e32 v136, v141
	v_mov_b32_e32 v137, v142
	v_mov_b32_e32 v141, v143
	v_pk_add_f32 v[136:137], v[136:137], v[140:141]
	v_pk_mul_f32 v[10:11], v[134:135], v[10:11]
	v_add_f32_e32 v136, v136, v137
	v_fmamk_f32 v136, v136, 0x3c000000, v205
	v_pk_mul_f32 v[8:9], v[132:133], v[8:9]
	v_pk_mul_f32 v[18:19], v[130:131], v[18:19]
	v_pk_mul_f32 v[16:17], v[128:129], v[16:17]
	v_rsq_f32_e32 v136, v136
	s_nop 0
	v_add_u32_e32 v140, s66, v199
	v_pk_mul_f32 v[48:49], v[48:49], v[136:137] op_sel_hi:[1,0]
	v_pk_mul_f32 v[50:51], v[50:51], v[136:137] op_sel_hi:[1,0]
	v_pk_mul_f32 v[64:65], v[64:65], v[136:137] op_sel_hi:[1,0]
	v_pk_mul_f32 v[66:67], v[66:67], v[136:137] op_sel_hi:[1,0]
	ds_read_b128 v[136:139], v140
	ds_read_b128 v[140:143], v140 offset:16
	v_pk_mul_f32 v[50:51], v[134:135], v[50:51]
	v_pk_mul_f32 v[48:49], v[132:133], v[48:49]
	v_pk_mul_f32 v[66:67], v[130:131], v[66:67]
	s_waitcnt lgkmcnt(1)
	v_mov_b32_e32 v174, v137
	v_mov_b32_e32 v175, v138
	v_mov_b32_e32 v137, v139
	v_pk_add_f32 v[136:137], v[174:175], v[136:137]
	v_pk_mul_f32 v[64:65], v[128:129], v[64:65]
	v_add_f32_e32 v136, v136, v137
	v_fmamk_f32 v136, v136, 0x3c000000, v205
	v_rsq_f32_e32 v136, v136
	s_nop 0
	v_pk_mul_f32 v[56:57], v[56:57], v[136:137] op_sel_hi:[1,0]
	v_pk_mul_f32 v[58:59], v[58:59], v[136:137] op_sel_hi:[1,0]
	v_pk_mul_f32 v[72:73], v[72:73], v[136:137] op_sel_hi:[1,0]
	v_pk_mul_f32 v[74:75], v[74:75], v[136:137] op_sel_hi:[1,0]
	s_waitcnt lgkmcnt(0)
	v_mov_b32_e32 v136, v141
	v_mov_b32_e32 v137, v142
	v_mov_b32_e32 v141, v143
	v_pk_add_f32 v[136:137], v[136:137], v[140:141]
	v_pk_mul_f32 v[58:59], v[134:135], v[58:59]
	v_add_f32_e32 v136, v136, v137
	v_fmamk_f32 v136, v136, 0x3c000000, v205
	v_pk_mul_f32 v[56:57], v[132:133], v[56:57]
	v_pk_mul_f32 v[74:75], v[130:131], v[74:75]
	v_pk_mul_f32 v[72:73], v[128:129], v[72:73]
	v_rsq_f32_e32 v136, v136
	s_nop 0
	v_add_u32_e32 v140, s67, v199
	v_pk_mul_f32 v[108:109], v[108:109], v[136:137] op_sel_hi:[1,0]
	v_pk_mul_f32 v[110:111], v[110:111], v[136:137] op_sel_hi:[1,0]
	v_pk_mul_f32 v[116:117], v[116:117], v[136:137] op_sel_hi:[1,0]
	v_pk_mul_f32 v[118:119], v[118:119], v[136:137] op_sel_hi:[1,0]
	ds_read_b128 v[136:139], v140
	ds_read_b128 v[140:143], v140 offset:16
	v_pk_mul_f32 v[110:111], v[134:135], v[110:111]
	v_pk_mul_f32 v[108:109], v[132:133], v[108:109]
	v_pk_mul_f32 v[118:119], v[130:131], v[118:119]
	s_waitcnt lgkmcnt(1)
	v_mov_b32_e32 v174, v137
	v_mov_b32_e32 v175, v138
	v_mov_b32_e32 v137, v139
	v_pk_add_f32 v[136:137], v[174:175], v[136:137]
	v_pk_mul_f32 v[116:117], v[128:129], v[116:117]
	v_add_f32_e32 v136, v136, v137
	v_fmamk_f32 v136, v136, 0x3c000000, v205
	v_rsq_f32_e32 v136, v136
	s_nop 0
	v_pk_mul_f32 v[32:33], v[32:33], v[136:137] op_sel_hi:[1,0]
	v_pk_mul_f32 v[34:35], v[34:35], v[136:137] op_sel_hi:[1,0]
	v_pk_mul_f32 v[40:41], v[40:41], v[136:137] op_sel_hi:[1,0]
	v_pk_mul_f32 v[42:43], v[42:43], v[136:137] op_sel_hi:[1,0]
	s_waitcnt lgkmcnt(0)
	v_mov_b32_e32 v136, v141
	v_mov_b32_e32 v137, v142
	v_mov_b32_e32 v141, v143
	v_pk_add_f32 v[136:137], v[136:137], v[140:141]
	v_pk_mul_f32 v[34:35], v[134:135], v[34:35]
	v_add_f32_e32 v136, v136, v137
	v_fmamk_f32 v136, v136, 0x3c000000, v205
	v_pk_mul_f32 v[32:33], v[132:133], v[32:33]
	v_pk_mul_f32 v[42:43], v[130:131], v[42:43]
	v_pk_mul_f32 v[40:41], v[128:129], v[40:41]
	v_rsq_f32_e32 v136, v136
	s_nop 0
	v_add_u32_e32 v140, s68, v199
	v_pk_mul_f32 v[88:89], v[88:89], v[136:137] op_sel_hi:[1,0]
	v_pk_mul_f32 v[90:91], v[90:91], v[136:137] op_sel_hi:[1,0]
	v_pk_mul_f32 v[100:101], v[100:101], v[136:137] op_sel_hi:[1,0]
	v_pk_mul_f32 v[102:103], v[102:103], v[136:137] op_sel_hi:[1,0]
	ds_read_b128 v[136:139], v140
	ds_read_b128 v[140:143], v140 offset:16
	v_pk_mul_f32 v[90:91], v[134:135], v[90:91]
	v_pk_mul_f32 v[88:89], v[132:133], v[88:89]
	v_pk_mul_f32 v[102:103], v[130:131], v[102:103]
	s_waitcnt lgkmcnt(1)
	v_mov_b32_e32 v174, v137
	v_mov_b32_e32 v175, v138
	v_mov_b32_e32 v137, v139
	v_pk_add_f32 v[136:137], v[174:175], v[136:137]
	v_pk_mul_f32 v[100:101], v[128:129], v[100:101]
	v_add_f32_e32 v136, v136, v137
	v_fmamk_f32 v136, v136, 0x3c000000, v205
	v_rsq_f32_e32 v136, v136
	s_nop 0
	v_pk_mul_f32 v[12:13], v[12:13], v[136:137] op_sel_hi:[1,0]
	v_pk_mul_f32 v[14:15], v[14:15], v[136:137] op_sel_hi:[1,0]
	v_pk_mul_f32 v[20:21], v[20:21], v[136:137] op_sel_hi:[1,0]
	v_pk_mul_f32 v[22:23], v[22:23], v[136:137] op_sel_hi:[1,0]
	s_waitcnt lgkmcnt(0)
	v_mov_b32_e32 v136, v141
	v_mov_b32_e32 v137, v142
	v_mov_b32_e32 v141, v143
	v_pk_add_f32 v[136:137], v[136:137], v[140:141]
	v_pk_mul_f32 v[14:15], v[134:135], v[14:15]
	v_add_f32_e32 v136, v136, v137
	v_fmamk_f32 v136, v136, 0x3c000000, v205
	v_pk_mul_f32 v[12:13], v[132:133], v[12:13]
	v_pk_mul_f32 v[22:23], v[130:131], v[22:23]
	v_pk_mul_f32 v[20:21], v[128:129], v[20:21]
	v_rsq_f32_e32 v136, v136
	s_nop 0
	v_add_u32_e32 v140, s69, v199
	v_pk_mul_f32 v[60:61], v[60:61], v[136:137] op_sel_hi:[1,0]
	v_pk_mul_f32 v[62:63], v[62:63], v[136:137] op_sel_hi:[1,0]
	v_pk_mul_f32 v[76:77], v[76:77], v[136:137] op_sel_hi:[1,0]
	v_pk_mul_f32 v[78:79], v[78:79], v[136:137] op_sel_hi:[1,0]
	ds_read_b128 v[136:139], v140
	ds_read_b128 v[140:143], v140 offset:16
	v_pk_mul_f32 v[62:63], v[134:135], v[62:63]
	v_pk_mul_f32 v[60:61], v[132:133], v[60:61]
	v_pk_mul_f32 v[78:79], v[130:131], v[78:79]
	s_waitcnt lgkmcnt(1)
	v_mov_b32_e32 v174, v137
	v_mov_b32_e32 v175, v138
	v_mov_b32_e32 v137, v139
	v_pk_add_f32 v[136:137], v[174:175], v[136:137]
	v_pk_mul_f32 v[76:77], v[128:129], v[76:77]
	v_add_f32_e32 v136, v136, v137
	v_fmamk_f32 v136, v136, 0x3c000000, v205
	v_rsq_f32_e32 v136, v136
	s_nop 0
	v_pk_mul_f32 v[0:1], v[0:1], v[136:137] op_sel_hi:[1,0]
	v_pk_mul_f32 v[2:3], v[2:3], v[136:137] op_sel_hi:[1,0]
	v_pk_mul_f32 v[4:5], v[4:5], v[136:137] op_sel_hi:[1,0]
	v_pk_mul_f32 v[6:7], v[6:7], v[136:137] op_sel_hi:[1,0]
	s_waitcnt lgkmcnt(0)
	v_mov_b32_e32 v136, v141
	v_mov_b32_e32 v137, v142
	v_mov_b32_e32 v141, v143
	v_pk_add_f32 v[136:137], v[136:137], v[140:141]
	v_pk_mul_f32 v[2:3], v[134:135], v[2:3]
	v_add_f32_e32 v136, v136, v137
	v_fmamk_f32 v136, v136, 0x3c000000, v205
	v_pk_mul_f32 v[0:1], v[132:133], v[0:1]
	v_pk_mul_f32 v[6:7], v[130:131], v[6:7]
	v_pk_mul_f32 v[4:5], v[128:129], v[4:5]
	s_cselect_b64 s[14:15], -1, 0
	s_or_b64 s[14:15], s[26:27], s[14:15]
	v_rsq_f32_e32 v136, v136
	s_nop 0
	v_pk_mul_f32 v[24:25], v[24:25], v[136:137] op_sel_hi:[1,0]
	v_pk_mul_f32 v[26:27], v[26:27], v[136:137] op_sel_hi:[1,0]
	v_pk_mul_f32 v[44:45], v[44:45], v[136:137] op_sel_hi:[1,0]
	v_pk_mul_f32 v[46:47], v[46:47], v[136:137] op_sel_hi:[1,0]
	v_pk_mul_f32 v[26:27], v[134:135], v[26:27]
	v_pk_mul_f32 v[24:25], v[132:133], v[24:25]
	v_pk_mul_f32 v[46:47], v[130:131], v[46:47]
	v_pk_mul_f32 v[44:45], v[128:129], v[44:45]
	s_and_b64 vcc, exec, s[14:15]
	s_cbranch_vccnz .LBB0_372
;     __device__ __forceinline__ void operator()(Acc& acc, const Unit& u, int wr, int wc, int fr, int fq, LAS unsigned char* le, int wid, int lane, int& cpm) const {
;     ...
;             if (type >= 3 && wc == 0) {
; #pragma unroll
;                 for (int ai = 0; ai < 2; ++ai)
; #pragma unroll
;                     for (int m = 0; m < 4; ++m) {
;                         const int pos = (row0 + ai * 128 + wr * 64 + m * 16 + fr) & (SEQ - 1);
;                         const float* cp = rope + (size_t)pos * 16 + (fq & 1) * 8;
;                         const f32x4 c0 = *(const f32x4*)cp, c1 = *(const f32x4*)(cp + 4), s0 = *(const f32x4*)(cp + SEQ * 16), s1 = *(const f32x4*)(cp + SEQ * 16 + 4);
; #pragma unroll
;                         for (int bj = 0; bj < 2; ++bj) {
;                             f32x4 a = acc[ai][bj][m][0], b = acc[ai][bj][m][1], oa, ob;
; #pragma unroll
;                             for (int j = 0; j < 4; ++j) { oa[j] = __shfl_xor(a[j], 32); ob[j] = __shfl_xor(b[j], 32); }
;                             if (fq < 2) { a = a * c0 - oa * s0; b = b * c1 - ob * s1; } else { a = a * c0 + oa * s0; b = b * c1 + ob * s1; }
;                             acc[ai][bj][m][0] = a; acc[ai][bj][m][1] = b;
;                         }
;                     }
;             }
	v_readlane_b32 s14, v254, 16
	s_add_i32 s16, s52, s14
	s_and_b32 s14, s16, 0xfc0
	v_or_b32_e32 v128, s14, v192
	v_lshlrev_b32_e32 v156, 6, v128
	v_lshl_add_u64 v[174:175], v[166:167], 0, v[156:157]
	v_add_co_u32_e32 v132, vcc, 0x40000, v174
	global_load_dwordx4 v[128:131], v[174:175], off offset:16
	global_load_dwordx4 v[140:143], v[174:175], off
	v_addc_co_u32_e32 v133, vcc, 0, v175, vcc
	global_load_dwordx4 v[136:139], v[132:133], off
	v_lshl_add_u64 v[132:133], v[174:175], 0, s[28:29]
	global_load_dwordx4 v[132:135], v[132:133], off offset:16
	ds_bpermute_b32 v184, v198, v80
	ds_bpermute_b32 v186, v198, v92
	ds_bpermute_b32 v185, v198, v81
	ds_bpermute_b32 v187, v198, v93
	ds_bpermute_b32 v190, v198, v82
	ds_bpermute_b32 v208, v198, v94
	ds_bpermute_b32 v191, v198, v83
	ds_bpermute_b32 v209, v198, v95
	s_waitcnt vmcnt(3)
	v_pk_mul_f32 v[180:181], v[94:95], v[130:131]
	s_waitcnt vmcnt(2)
	v_pk_mul_f32 v[176:177], v[82:83], v[142:143]
	v_pk_mul_f32 v[178:179], v[80:81], v[140:141]
	v_pk_mul_f32 v[182:183], v[92:93], v[128:129]
	s_waitcnt vmcnt(1) lgkmcnt(5)
	v_pk_mul_f32 v[188:189], v[136:137], v[184:185]
	s_waitcnt lgkmcnt(1)
	v_pk_mul_f32 v[190:191], v[138:139], v[190:191]
	s_waitcnt vmcnt(0) lgkmcnt(0)
	v_pk_mul_f32 v[184:185], v[134:135], v[208:209]
	v_pk_mul_f32 v[186:187], v[132:133], v[186:187]
	s_and_saveexec_b64 s[14:15], s[10:11]
	s_xor_b64 s[14:15], exec, s[14:15]
	v_pk_add_f32 v[82:83], v[176:177], v[190:191]
	v_pk_add_f32 v[80:81], v[178:179], v[188:189]
	v_pk_add_f32 v[94:95], v[180:181], v[184:185]
	v_pk_add_f32 v[92:93], v[182:183], v[186:187]
	s_andn2_saveexec_b64 s[14:15], s[14:15]
	v_sub_f32_e32 v83, v177, v191
	v_sub_f32_e32 v82, v176, v190
	v_sub_f32_e32 v81, v179, v189
	v_sub_f32_e32 v80, v178, v188
	v_sub_f32_e32 v95, v181, v185
	v_sub_f32_e32 v94, v180, v184
	v_sub_f32_e32 v93, v183, v187
	v_sub_f32_e32 v92, v182, v186
	s_or_b64 exec, exec, s[14:15]
	ds_bpermute_b32 v176, v198, v120
	ds_bpermute_b32 v178, v198, v124
	ds_bpermute_b32 v177, v198, v121
	ds_bpermute_b32 v179, v198, v125
	ds_bpermute_b32 v180, v198, v122
	ds_bpermute_b32 v181, v198, v123
	ds_bpermute_b32 v182, v198, v126
	ds_bpermute_b32 v183, v198, v127
	v_pk_mul_f32 v[142:143], v[122:123], v[142:143]
	v_pk_mul_f32 v[140:141], v[120:121], v[140:141]
	s_waitcnt lgkmcnt(2)
	v_pk_mul_f32 v[138:139], v[138:139], v[180:181]
	v_pk_mul_f32 v[136:137], v[136:137], v[176:177]
	v_pk_mul_f32 v[130:131], v[126:127], v[130:131]
	v_pk_mul_f32 v[128:129], v[124:125], v[128:129]
	s_waitcnt lgkmcnt(0)
	v_pk_mul_f32 v[134:135], v[134:135], v[182:183]
	v_pk_mul_f32 v[132:133], v[132:133], v[178:179]
	s_and_saveexec_b64 s[14:15], s[10:11]
	s_xor_b64 s[14:15], exec, s[14:15]
	v_pk_add_f32 v[122:123], v[142:143], v[138:139]
	v_pk_add_f32 v[120:121], v[140:141], v[136:137]
	v_pk_add_f32 v[126:127], v[130:131], v[134:135]
	v_pk_add_f32 v[124:125], v[128:129], v[132:133]
	s_andn2_saveexec_b64 s[14:15], s[14:15]
	v_sub_f32_e32 v123, v143, v139
	v_sub_f32_e32 v122, v142, v138
	v_sub_f32_e32 v121, v141, v137
	v_sub_f32_e32 v120, v140, v136
	v_sub_f32_e32 v127, v131, v135
	v_sub_f32_e32 v126, v130, v134
	v_sub_f32_e32 v125, v129, v133
	v_sub_f32_e32 v124, v128, v132
	s_or_b64 exec, exec, s[14:15]
	v_add_co_u32_e32 v132, vcc, 0x40000, v174
	global_load_dwordx4 v[128:131], v[174:175], off offset:1040
	global_load_dwordx4 v[140:143], v[174:175], off offset:1024
	v_addc_co_u32_e32 v133, vcc, 0, v175, vcc
	global_load_dwordx4 v[136:139], v[132:133], off offset:1024
	v_lshl_add_u64 v[132:133], v[174:175], 0, s[30:31]
	global_load_dwordx4 v[132:135], v[132:133], off offset:16
	ds_bpermute_b32 v184, v198, v52
	ds_bpermute_b32 v186, v198, v68
	ds_bpermute_b32 v185, v198, v53
	ds_bpermute_b32 v187, v198, v69
	ds_bpermute_b32 v190, v198, v54
	ds_bpermute_b32 v208, v198, v70
	ds_bpermute_b32 v191, v198, v55
	ds_bpermute_b32 v209, v198, v71
	s_waitcnt vmcnt(3)
	v_pk_mul_f32 v[180:181], v[70:71], v[130:131]
	s_waitcnt vmcnt(2)
	v_pk_mul_f32 v[176:177], v[54:55], v[142:143]
	v_pk_mul_f32 v[178:179], v[52:53], v[140:141]
	v_pk_mul_f32 v[182:183], v[68:69], v[128:129]
	s_waitcnt vmcnt(1) lgkmcnt(5)
	v_pk_mul_f32 v[188:189], v[136:137], v[184:185]
	s_waitcnt lgkmcnt(1)
	v_pk_mul_f32 v[190:191], v[138:139], v[190:191]
	s_waitcnt vmcnt(0) lgkmcnt(0)
	v_pk_mul_f32 v[184:185], v[134:135], v[208:209]
	v_pk_mul_f32 v[186:187], v[132:133], v[186:187]
	s_and_saveexec_b64 s[14:15], s[10:11]
	s_xor_b64 s[14:15], exec, s[14:15]
	v_pk_add_f32 v[54:55], v[176:177], v[190:191]
	v_pk_add_f32 v[52:53], v[178:179], v[188:189]
	v_pk_add_f32 v[70:71], v[180:181], v[184:185]
	v_pk_add_f32 v[68:69], v[182:183], v[186:187]
	s_andn2_saveexec_b64 s[14:15], s[14:15]
	v_sub_f32_e32 v55, v177, v191
	v_sub_f32_e32 v54, v176, v190
	v_sub_f32_e32 v53, v179, v189
	v_sub_f32_e32 v52, v178, v188
	v_sub_f32_e32 v71, v181, v185
	v_sub_f32_e32 v70, v180, v184
	v_sub_f32_e32 v69, v183, v187
	v_sub_f32_e32 v68, v182, v186
	s_or_b64 exec, exec, s[14:15]
	ds_bpermute_b32 v176, v198, v104
	ds_bpermute_b32 v178, v198, v112
	ds_bpermute_b32 v177, v198, v105
	ds_bpermute_b32 v179, v198, v113
	ds_bpermute_b32 v180, v198, v106
	ds_bpermute_b32 v181, v198, v107
	ds_bpermute_b32 v182, v198, v114
	ds_bpermute_b32 v183, v198, v115
	v_pk_mul_f32 v[142:143], v[106:107], v[142:143]
	v_pk_mul_f32 v[140:141], v[104:105], v[140:141]
	s_waitcnt lgkmcnt(2)
	v_pk_mul_f32 v[138:139], v[138:139], v[180:181]
	v_pk_mul_f32 v[136:137], v[136:137], v[176:177]
	v_pk_mul_f32 v[130:131], v[114:115], v[130:131]
	v_pk_mul_f32 v[128:129], v[112:113], v[128:129]
	s_waitcnt lgkmcnt(0)
;     __device__ __forceinline__ void operator()(Acc& acc, const Unit& u, int wr, int wc, int fr, int fq, LAS unsigned char* le, int wid, int lane, int& cpm) const {
;     ...
;                     for (int m = 0; m < 4; ++m) {
;                         const int pos = (row0 + ai * 128 + wr * 64 + m * 16 + fr) & (SEQ - 1);
;                         const float* cp = rope + (size_t)pos * 16 + (fq & 1) * 8;
;                         const f32x4 c0 = *(const f32x4*)cp, c1 = *(const f32x4*)(cp + 4), s0 = *(const f32x4*)(cp + SEQ * 16), s1 = *(const f32x4*)(cp + SEQ * 16 + 4);
; #pragma unroll
;                         for (int bj = 0; bj < 2; ++bj) {
;                             f32x4 a = acc[ai][bj][m][0], b = acc[ai][bj][m][1], oa, ob;
; #pragma unroll
;                             for (int j = 0; j < 4; ++j) { oa[j] = __shfl_xor(a[j], 32); ob[j] = __shfl_xor(b[j], 32); }
;                             if (fq < 2) { a = a * c0 - oa * s0; b = b * c1 - ob * s1; } else { a = a * c0 + oa * s0; b = b * c1 + ob * s1; }
;                             acc[ai][bj][m][0] = a; acc[ai][bj][m][1] = b;
;                         }
;                     }
	v_pk_mul_f32 v[134:135], v[134:135], v[182:183]
	v_pk_mul_f32 v[132:133], v[132:133], v[178:179]
	s_and_saveexec_b64 s[14:15], s[10:11]
	s_xor_b64 s[14:15], exec, s[14:15]
	v_pk_add_f32 v[106:107], v[142:143], v[138:139]
	v_pk_add_f32 v[104:105], v[140:141], v[136:137]
	v_pk_add_f32 v[114:115], v[130:131], v[134:135]
	v_pk_add_f32 v[112:113], v[128:129], v[132:133]
	s_andn2_saveexec_b64 s[14:15], s[14:15]
	v_sub_f32_e32 v107, v143, v139
	v_sub_f32_e32 v106, v142, v138
	v_sub_f32_e32 v105, v141, v137
	v_sub_f32_e32 v104, v140, v136
	v_sub_f32_e32 v115, v131, v135
	v_sub_f32_e32 v114, v130, v134
	v_sub_f32_e32 v113, v129, v133
	v_sub_f32_e32 v112, v128, v132
	s_or_b64 exec, exec, s[14:15]
	v_add_co_u32_e32 v132, vcc, 0x40000, v174
	global_load_dwordx4 v[128:131], v[174:175], off offset:2064
	global_load_dwordx4 v[140:143], v[174:175], off offset:2048
	v_addc_co_u32_e32 v133, vcc, 0, v175, vcc
	global_load_dwordx4 v[136:139], v[132:133], off offset:2048
	v_lshl_add_u64 v[132:133], v[174:175], 0, s[34:35]
	global_load_dwordx4 v[132:135], v[132:133], off offset:16
	ds_bpermute_b32 v184, v198, v28
	ds_bpermute_b32 v186, v198, v36
	ds_bpermute_b32 v185, v198, v29
	ds_bpermute_b32 v187, v198, v37
	ds_bpermute_b32 v190, v198, v30
	ds_bpermute_b32 v208, v198, v38
	ds_bpermute_b32 v191, v198, v31
	ds_bpermute_b32 v209, v198, v39
	s_waitcnt vmcnt(3)
	v_pk_mul_f32 v[180:181], v[38:39], v[130:131]
	s_waitcnt vmcnt(2)
	v_pk_mul_f32 v[176:177], v[30:31], v[142:143]
	v_pk_mul_f32 v[178:179], v[28:29], v[140:141]
	v_pk_mul_f32 v[182:183], v[36:37], v[128:129]
	s_waitcnt vmcnt(1) lgkmcnt(5)
	v_pk_mul_f32 v[188:189], v[136:137], v[184:185]
	s_waitcnt lgkmcnt(1)
	v_pk_mul_f32 v[190:191], v[138:139], v[190:191]
	s_waitcnt vmcnt(0) lgkmcnt(0)
	v_pk_mul_f32 v[184:185], v[134:135], v[208:209]
	v_pk_mul_f32 v[186:187], v[132:133], v[186:187]
	s_and_saveexec_b64 s[14:15], s[10:11]
	s_xor_b64 s[14:15], exec, s[14:15]
	v_pk_add_f32 v[30:31], v[176:177], v[190:191]
	v_pk_add_f32 v[28:29], v[178:179], v[188:189]
	v_pk_add_f32 v[38:39], v[180:181], v[184:185]
	v_pk_add_f32 v[36:37], v[182:183], v[186:187]
	s_andn2_saveexec_b64 s[14:15], s[14:15]
	v_sub_f32_e32 v31, v177, v191
	v_sub_f32_e32 v30, v176, v190
	v_sub_f32_e32 v29, v179, v189
	v_sub_f32_e32 v28, v178, v188
	v_sub_f32_e32 v39, v181, v185
	v_sub_f32_e32 v38, v180, v184
	v_sub_f32_e32 v37, v183, v187
	v_sub_f32_e32 v36, v182, v186
	s_or_b64 exec, exec, s[14:15]
	ds_bpermute_b32 v176, v198, v84
	ds_bpermute_b32 v178, v198, v96
	ds_bpermute_b32 v177, v198, v85
	ds_bpermute_b32 v179, v198, v97
	ds_bpermute_b32 v180, v198, v86
	ds_bpermute_b32 v181, v198, v87
	ds_bpermute_b32 v182, v198, v98
	ds_bpermute_b32 v183, v198, v99
	v_pk_mul_f32 v[142:143], v[86:87], v[142:143]
	v_pk_mul_f32 v[140:141], v[84:85], v[140:141]
	s_waitcnt lgkmcnt(2)
	v_pk_mul_f32 v[138:139], v[138:139], v[180:181]
	v_pk_mul_f32 v[136:137], v[136:137], v[176:177]
	v_pk_mul_f32 v[130:131], v[98:99], v[130:131]
	v_pk_mul_f32 v[128:129], v[96:97], v[128:129]
	s_waitcnt lgkmcnt(0)
	v_pk_mul_f32 v[134:135], v[134:135], v[182:183]
	v_pk_mul_f32 v[132:133], v[132:133], v[178:179]
	s_and_saveexec_b64 s[14:15], s[10:11]
	s_xor_b64 s[14:15], exec, s[14:15]
	v_pk_add_f32 v[86:87], v[142:143], v[138:139]
	v_pk_add_f32 v[84:85], v[140:141], v[136:137]
	v_pk_add_f32 v[98:99], v[130:131], v[134:135]
	v_pk_add_f32 v[96:97], v[128:129], v[132:133]
	s_andn2_saveexec_b64 s[14:15], s[14:15]
	v_sub_f32_e32 v87, v143, v139
	v_sub_f32_e32 v86, v142, v138
	v_sub_f32_e32 v85, v141, v137
	v_sub_f32_e32 v84, v140, v136
	v_sub_f32_e32 v99, v131, v135
	v_sub_f32_e32 v98, v130, v134
	v_sub_f32_e32 v97, v129, v133
	v_sub_f32_e32 v96, v128, v132
	s_or_b64 exec, exec, s[14:15]
	v_add_co_u32_e32 v132, vcc, 0x40000, v174
	global_load_dwordx4 v[128:131], v[174:175], off offset:3088
	global_load_dwordx4 v[140:143], v[174:175], off offset:3072
	v_addc_co_u32_e32 v133, vcc, 0, v175, vcc
	global_load_dwordx4 v[136:139], v[132:133], off offset:3072
	v_lshl_add_u64 v[132:133], v[174:175], 0, s[36:37]
	global_load_dwordx4 v[132:135], v[132:133], off offset:16
	ds_bpermute_b32 v182, v198, v8
	ds_bpermute_b32 v184, v198, v16
	ds_bpermute_b32 v183, v198, v9
	ds_bpermute_b32 v185, v198, v17
	ds_bpermute_b32 v188, v198, v10
	ds_bpermute_b32 v190, v198, v18
	ds_bpermute_b32 v189, v198, v11
	ds_bpermute_b32 v191, v198, v19
	s_waitcnt vmcnt(3)
	v_pk_mul_f32 v[178:179], v[18:19], v[130:131]
	s_waitcnt vmcnt(2)
	v_pk_mul_f32 v[174:175], v[10:11], v[142:143]
	v_pk_mul_f32 v[176:177], v[8:9], v[140:141]
	v_pk_mul_f32 v[180:181], v[16:17], v[128:129]
	s_waitcnt vmcnt(1) lgkmcnt(5)
	v_pk_mul_f32 v[186:187], v[136:137], v[182:183]
	s_waitcnt lgkmcnt(1)
	v_pk_mul_f32 v[188:189], v[138:139], v[188:189]
	s_waitcnt vmcnt(0) lgkmcnt(0)
	v_pk_mul_f32 v[182:183], v[134:135], v[190:191]
	v_pk_mul_f32 v[184:185], v[132:133], v[184:185]
	s_and_saveexec_b64 s[14:15], s[10:11]
	s_xor_b64 s[14:15], exec, s[14:15]
	v_pk_add_f32 v[10:11], v[174:175], v[188:189]
	v_pk_add_f32 v[8:9], v[176:177], v[186:187]
	v_pk_add_f32 v[18:19], v[178:179], v[182:183]
	v_pk_add_f32 v[16:17], v[180:181], v[184:185]
	s_andn2_saveexec_b64 s[14:15], s[14:15]
	v_sub_f32_e32 v11, v175, v189
	v_sub_f32_e32 v10, v174, v188
	v_sub_f32_e32 v9, v177, v187
	v_sub_f32_e32 v8, v176, v186
	v_sub_f32_e32 v19, v179, v183
	v_sub_f32_e32 v18, v178, v182
	v_sub_f32_e32 v17, v181, v185
	v_sub_f32_e32 v16, v180, v184
	s_or_b64 exec, exec, s[14:15]
	ds_bpermute_b32 v174, v198, v48
	ds_bpermute_b32 v176, v198, v64
	ds_bpermute_b32 v175, v198, v49
	ds_bpermute_b32 v177, v198, v65
	ds_bpermute_b32 v178, v198, v50
	ds_bpermute_b32 v179, v198, v51
	ds_bpermute_b32 v180, v198, v66
	ds_bpermute_b32 v181, v198, v67
	v_pk_mul_f32 v[142:143], v[50:51], v[142:143]
	v_pk_mul_f32 v[140:141], v[48:49], v[140:141]
	s_waitcnt lgkmcnt(2)
;     __device__ __forceinline__ void operator()(Acc& acc, const Unit& u, int wr, int wc, int fr, int fq, LAS unsigned char* le, int wid, int lane, int& cpm) const {
;     ...
;                     for (int m = 0; m < 4; ++m) {
;                         const int pos = (row0 + ai * 128 + wr * 64 + m * 16 + fr) & (SEQ - 1);
;                         const float* cp = rope + (size_t)pos * 16 + (fq & 1) * 8;
;                         const f32x4 c0 = *(const f32x4*)cp, c1 = *(const f32x4*)(cp + 4), s0 = *(const f32x4*)(cp + SEQ * 16), s1 = *(const f32x4*)(cp + SEQ * 16 + 4);
; #pragma unroll
;                         for (int bj = 0; bj < 2; ++bj) {
;                             f32x4 a = acc[ai][bj][m][0], b = acc[ai][bj][m][1], oa, ob;
; #pragma unroll
;                             for (int j = 0; j < 4; ++j) { oa[j] = __shfl_xor(a[j], 32); ob[j] = __shfl_xor(b[j], 32); }
;                             if (fq < 2) { a = a * c0 - oa * s0; b = b * c1 - ob * s1; } else { a = a * c0 + oa * s0; b = b * c1 + ob * s1; }
;                             acc[ai][bj][m][0] = a; acc[ai][bj][m][1] = b;
;                         }
;                     }
	v_pk_mul_f32 v[138:139], v[138:139], v[178:179]
	v_pk_mul_f32 v[136:137], v[136:137], v[174:175]
	v_pk_mul_f32 v[130:131], v[66:67], v[130:131]
	v_pk_mul_f32 v[128:129], v[64:65], v[128:129]
	s_waitcnt lgkmcnt(0)
	v_pk_mul_f32 v[134:135], v[134:135], v[180:181]
	v_pk_mul_f32 v[132:133], v[132:133], v[176:177]
	s_and_saveexec_b64 s[14:15], s[10:11]
	s_xor_b64 s[14:15], exec, s[14:15]
	v_pk_add_f32 v[50:51], v[142:143], v[138:139]
	v_pk_add_f32 v[48:49], v[140:141], v[136:137]
	v_pk_add_f32 v[66:67], v[130:131], v[134:135]
	v_pk_add_f32 v[64:65], v[128:129], v[132:133]
	s_andn2_saveexec_b64 s[14:15], s[14:15]
	v_sub_f32_e32 v51, v143, v139
	v_sub_f32_e32 v50, v142, v138
	v_sub_f32_e32 v49, v141, v137
	v_sub_f32_e32 v48, v140, v136
	v_sub_f32_e32 v67, v131, v135
	v_sub_f32_e32 v66, v130, v134
	v_sub_f32_e32 v65, v129, v133
	v_sub_f32_e32 v64, v128, v132
	s_or_b64 exec, exec, s[14:15]
	s_addk_i32 s16, 0x80
	s_and_b32 s14, s16, 0xfc0
	v_or_b32_e32 v128, s14, v192
	v_lshlrev_b32_e32 v156, 6, v128
	v_lshl_add_u64 v[174:175], v[166:167], 0, v[156:157]
	v_add_co_u32_e32 v132, vcc, 0x40000, v174
	global_load_dwordx4 v[128:131], v[174:175], off offset:16
	global_load_dwordx4 v[140:143], v[174:175], off
	v_addc_co_u32_e32 v133, vcc, 0, v175, vcc
	global_load_dwordx4 v[136:139], v[132:133], off
	v_lshl_add_u64 v[132:133], v[174:175], 0, s[28:29]
	global_load_dwordx4 v[132:135], v[132:133], off offset:16
	ds_bpermute_b32 v184, v198, v56
	ds_bpermute_b32 v186, v198, v72
	ds_bpermute_b32 v185, v198, v57
	ds_bpermute_b32 v187, v198, v73
	ds_bpermute_b32 v190, v198, v58
	ds_bpermute_b32 v208, v198, v74
	ds_bpermute_b32 v191, v198, v59
	ds_bpermute_b32 v209, v198, v75
	s_waitcnt vmcnt(3)
	v_pk_mul_f32 v[180:181], v[74:75], v[130:131]
	s_waitcnt vmcnt(2)
	v_pk_mul_f32 v[176:177], v[58:59], v[142:143]
	v_pk_mul_f32 v[178:179], v[56:57], v[140:141]
	v_pk_mul_f32 v[182:183], v[72:73], v[128:129]
	s_waitcnt vmcnt(1) lgkmcnt(5)
	v_pk_mul_f32 v[188:189], v[136:137], v[184:185]
	s_waitcnt lgkmcnt(1)
	v_pk_mul_f32 v[190:191], v[138:139], v[190:191]
	s_waitcnt vmcnt(0) lgkmcnt(0)
	v_pk_mul_f32 v[184:185], v[134:135], v[208:209]
	v_pk_mul_f32 v[186:187], v[132:133], v[186:187]
	s_and_saveexec_b64 s[14:15], s[10:11]
	s_xor_b64 s[14:15], exec, s[14:15]
	v_pk_add_f32 v[58:59], v[176:177], v[190:191]
	v_pk_add_f32 v[56:57], v[178:179], v[188:189]
	v_pk_add_f32 v[74:75], v[180:181], v[184:185]
	v_pk_add_f32 v[72:73], v[182:183], v[186:187]
	s_andn2_saveexec_b64 s[14:15], s[14:15]
	v_sub_f32_e32 v59, v177, v191
	v_sub_f32_e32 v58, v176, v190
	v_sub_f32_e32 v57, v179, v189
	v_sub_f32_e32 v56, v178, v188
	v_sub_f32_e32 v75, v181, v185
	v_sub_f32_e32 v74, v180, v184
	v_sub_f32_e32 v73, v183, v187
	v_sub_f32_e32 v72, v182, v186
	s_or_b64 exec, exec, s[14:15]
	ds_bpermute_b32 v176, v198, v108
	ds_bpermute_b32 v178, v198, v116
	ds_bpermute_b32 v177, v198, v109
	ds_bpermute_b32 v179, v198, v117
	ds_bpermute_b32 v180, v198, v110
	ds_bpermute_b32 v181, v198, v111
	ds_bpermute_b32 v182, v198, v118
	ds_bpermute_b32 v183, v198, v119
	v_pk_mul_f32 v[142:143], v[110:111], v[142:143]
	v_pk_mul_f32 v[140:141], v[108:109], v[140:141]
	s_waitcnt lgkmcnt(2)
	v_pk_mul_f32 v[138:139], v[138:139], v[180:181]
	v_pk_mul_f32 v[136:137], v[136:137], v[176:177]
	v_pk_mul_f32 v[130:131], v[118:119], v[130:131]
	v_pk_mul_f32 v[128:129], v[116:117], v[128:129]
	s_waitcnt lgkmcnt(0)
	v_pk_mul_f32 v[134:135], v[134:135], v[182:183]
	v_pk_mul_f32 v[132:133], v[132:133], v[178:179]
	s_and_saveexec_b64 s[14:15], s[10:11]
	s_xor_b64 s[14:15], exec, s[14:15]
	v_pk_add_f32 v[110:111], v[142:143], v[138:139]
	v_pk_add_f32 v[108:109], v[140:141], v[136:137]
	v_pk_add_f32 v[118:119], v[130:131], v[134:135]
	v_pk_add_f32 v[116:117], v[128:129], v[132:133]
	s_andn2_saveexec_b64 s[14:15], s[14:15]
	v_sub_f32_e32 v111, v143, v139
	v_sub_f32_e32 v110, v142, v138
	v_sub_f32_e32 v109, v141, v137
	v_sub_f32_e32 v108, v140, v136
	v_sub_f32_e32 v119, v131, v135
	v_sub_f32_e32 v118, v130, v134
	v_sub_f32_e32 v117, v129, v133
	v_sub_f32_e32 v116, v128, v132
	s_or_b64 exec, exec, s[14:15]
	v_add_co_u32_e32 v132, vcc, 0x40000, v174
	global_load_dwordx4 v[128:131], v[174:175], off offset:1040
	global_load_dwordx4 v[140:143], v[174:175], off offset:1024
	v_addc_co_u32_e32 v133, vcc, 0, v175, vcc
	global_load_dwordx4 v[136:139], v[132:133], off offset:1024
	v_lshl_add_u64 v[132:133], v[174:175], 0, s[30:31]
	global_load_dwordx4 v[132:135], v[132:133], off offset:16
	ds_bpermute_b32 v184, v198, v32
	ds_bpermute_b32 v186, v198, v40
	ds_bpermute_b32 v185, v198, v33
	ds_bpermute_b32 v187, v198, v41
	ds_bpermute_b32 v190, v198, v34
	ds_bpermute_b32 v208, v198, v42
	ds_bpermute_b32 v191, v198, v35
	ds_bpermute_b32 v209, v198, v43
	s_waitcnt vmcnt(3)
	v_pk_mul_f32 v[180:181], v[42:43], v[130:131]
	s_waitcnt vmcnt(2)
	v_pk_mul_f32 v[176:177], v[34:35], v[142:143]
	v_pk_mul_f32 v[178:179], v[32:33], v[140:141]
	v_pk_mul_f32 v[182:183], v[40:41], v[128:129]
	s_waitcnt vmcnt(1) lgkmcnt(5)
	v_pk_mul_f32 v[188:189], v[136:137], v[184:185]
	s_waitcnt lgkmcnt(1)
	v_pk_mul_f32 v[190:191], v[138:139], v[190:191]
	s_waitcnt vmcnt(0) lgkmcnt(0)
;     __device__ __forceinline__ void operator()(Acc& acc, const Unit& u, int wr, int wc, int fr, int fq, LAS unsigned char* le, int wid, int lane, int& cpm) const {
;     ...
;                     for (int m = 0; m < 4; ++m) {
;                         const int pos = (row0 + ai * 128 + wr * 64 + m * 16 + fr) & (SEQ - 1);
;                         const float* cp = rope + (size_t)pos * 16 + (fq & 1) * 8;
;                         const f32x4 c0 = *(const f32x4*)cp, c1 = *(const f32x4*)(cp + 4), s0 = *(const f32x4*)(cp + SEQ * 16), s1 = *(const f32x4*)(cp + SEQ * 16 + 4);
; #pragma unroll
;                         for (int bj = 0; bj < 2; ++bj) {
;                             f32x4 a = acc[ai][bj][m][0], b = acc[ai][bj][m][1], oa, ob;
; #pragma unroll
;                             for (int j = 0; j < 4; ++j) { oa[j] = __shfl_xor(a[j], 32); ob[j] = __shfl_xor(b[j], 32); }
;                             if (fq < 2) { a = a * c0 - oa * s0; b = b * c1 - ob * s1; } else { a = a * c0 + oa * s0; b = b * c1 + ob * s1; }
;                             acc[ai][bj][m][0] = a; acc[ai][bj][m][1] = b;
;                         }
;                     }
	v_pk_mul_f32 v[184:185], v[134:135], v[208:209]
	v_pk_mul_f32 v[186:187], v[132:133], v[186:187]
	s_and_saveexec_b64 s[14:15], s[10:11]
	s_xor_b64 s[14:15], exec, s[14:15]
	v_pk_add_f32 v[34:35], v[176:177], v[190:191]
	v_pk_add_f32 v[32:33], v[178:179], v[188:189]
	v_pk_add_f32 v[42:43], v[180:181], v[184:185]
	v_pk_add_f32 v[40:41], v[182:183], v[186:187]
	s_andn2_saveexec_b64 s[14:15], s[14:15]
	v_sub_f32_e32 v35, v177, v191
	v_sub_f32_e32 v34, v176, v190
	v_sub_f32_e32 v33, v179, v189
	v_sub_f32_e32 v32, v178, v188
	v_sub_f32_e32 v43, v181, v185
	v_sub_f32_e32 v42, v180, v184
	v_sub_f32_e32 v41, v183, v187
	v_sub_f32_e32 v40, v182, v186
	s_or_b64 exec, exec, s[14:15]
	ds_bpermute_b32 v176, v198, v88
	ds_bpermute_b32 v178, v198, v100
	ds_bpermute_b32 v177, v198, v89
	ds_bpermute_b32 v179, v198, v101
	ds_bpermute_b32 v180, v198, v90
	ds_bpermute_b32 v181, v198, v91
	ds_bpermute_b32 v182, v198, v102
	ds_bpermute_b32 v183, v198, v103
	v_pk_mul_f32 v[142:143], v[90:91], v[142:143]
	v_pk_mul_f32 v[140:141], v[88:89], v[140:141]
	s_waitcnt lgkmcnt(2)
	v_pk_mul_f32 v[138:139], v[138:139], v[180:181]
	v_pk_mul_f32 v[136:137], v[136:137], v[176:177]
	v_pk_mul_f32 v[130:131], v[102:103], v[130:131]
	v_pk_mul_f32 v[128:129], v[100:101], v[128:129]
	s_waitcnt lgkmcnt(0)
	v_pk_mul_f32 v[134:135], v[134:135], v[182:183]
	v_pk_mul_f32 v[132:133], v[132:133], v[178:179]
	s_and_saveexec_b64 s[14:15], s[10:11]
	s_xor_b64 s[14:15], exec, s[14:15]
	v_pk_add_f32 v[90:91], v[142:143], v[138:139]
	v_pk_add_f32 v[88:89], v[140:141], v[136:137]
	v_pk_add_f32 v[102:103], v[130:131], v[134:135]
	v_pk_add_f32 v[100:101], v[128:129], v[132:133]
	s_andn2_saveexec_b64 s[14:15], s[14:15]
	v_sub_f32_e32 v91, v143, v139
	v_sub_f32_e32 v90, v142, v138
	v_sub_f32_e32 v89, v141, v137
	v_sub_f32_e32 v88, v140, v136
	v_sub_f32_e32 v103, v131, v135
	v_sub_f32_e32 v102, v130, v134
	v_sub_f32_e32 v101, v129, v133
	v_sub_f32_e32 v100, v128, v132
	s_or_b64 exec, exec, s[14:15]
	v_add_co_u32_e32 v132, vcc, 0x40000, v174
	global_load_dwordx4 v[128:131], v[174:175], off offset:2064
	global_load_dwordx4 v[140:143], v[174:175], off offset:2048
	v_addc_co_u32_e32 v133, vcc, 0, v175, vcc
	global_load_dwordx4 v[136:139], v[132:133], off offset:2048
	v_lshl_add_u64 v[132:133], v[174:175], 0, s[34:35]
	global_load_dwordx4 v[132:135], v[132:133], off offset:16
	ds_bpermute_b32 v184, v198, v12
	ds_bpermute_b32 v186, v198, v20
	ds_bpermute_b32 v185, v198, v13
	ds_bpermute_b32 v187, v198, v21
	ds_bpermute_b32 v190, v198, v14
	ds_bpermute_b32 v208, v198, v22
	ds_bpermute_b32 v191, v198, v15
	ds_bpermute_b32 v209, v198, v23
	s_waitcnt vmcnt(3)
	v_pk_mul_f32 v[180:181], v[22:23], v[130:131]
	s_waitcnt vmcnt(2)
	v_pk_mul_f32 v[176:177], v[14:15], v[142:143]
	v_pk_mul_f32 v[178:179], v[12:13], v[140:141]
	v_pk_mul_f32 v[182:183], v[20:21], v[128:129]
	s_waitcnt vmcnt(1) lgkmcnt(5)
	v_pk_mul_f32 v[188:189], v[136:137], v[184:185]
	s_waitcnt lgkmcnt(1)
	v_pk_mul_f32 v[190:191], v[138:139], v[190:191]
	s_waitcnt vmcnt(0) lgkmcnt(0)
	v_pk_mul_f32 v[184:185], v[134:135], v[208:209]
	v_pk_mul_f32 v[186:187], v[132:133], v[186:187]
	s_and_saveexec_b64 s[14:15], s[10:11]
	s_xor_b64 s[14:15], exec, s[14:15]
	v_pk_add_f32 v[14:15], v[176:177], v[190:191]
	v_pk_add_f32 v[12:13], v[178:179], v[188:189]
	v_pk_add_f32 v[22:23], v[180:181], v[184:185]
	v_pk_add_f32 v[20:21], v[182:183], v[186:187]
	s_andn2_saveexec_b64 s[14:15], s[14:15]
	v_sub_f32_e32 v15, v177, v191
	v_sub_f32_e32 v14, v176, v190
	v_sub_f32_e32 v13, v179, v189
	v_sub_f32_e32 v12, v178, v188
	v_sub_f32_e32 v23, v181, v185
	v_sub_f32_e32 v22, v180, v184
	v_sub_f32_e32 v21, v183, v187
	v_sub_f32_e32 v20, v182, v186
	s_or_b64 exec, exec, s[14:15]
	ds_bpermute_b32 v176, v198, v60
	ds_bpermute_b32 v178, v198, v76
	ds_bpermute_b32 v177, v198, v61
	ds_bpermute_b32 v179, v198, v77
	ds_bpermute_b32 v180, v198, v62
	ds_bpermute_b32 v181, v198, v63
	ds_bpermute_b32 v182, v198, v78
	ds_bpermute_b32 v183, v198, v79
	v_pk_mul_f32 v[142:143], v[62:63], v[142:143]
	v_pk_mul_f32 v[140:141], v[60:61], v[140:141]
	s_waitcnt lgkmcnt(2)
;     __device__ __forceinline__ void operator()(Acc& acc, const Unit& u, int wr, int wc, int fr, int fq, LAS unsigned char* le, int wid, int lane, int& cpm) const {
;     ...
;                     for (int m = 0; m < 4; ++m) {
;                         const int pos = (row0 + ai * 128 + wr * 64 + m * 16 + fr) & (SEQ - 1);
;                         const float* cp = rope + (size_t)pos * 16 + (fq & 1) * 8;
;                         const f32x4 c0 = *(const f32x4*)cp, c1 = *(const f32x4*)(cp + 4), s0 = *(const f32x4*)(cp + SEQ * 16), s1 = *(const f32x4*)(cp + SEQ * 16 + 4);
; #pragma unroll
;                         for (int bj = 0; bj < 2; ++bj) {
;                             f32x4 a = acc[ai][bj][m][0], b = acc[ai][bj][m][1], oa, ob;
; #pragma unroll
;                             for (int j = 0; j < 4; ++j) { oa[j] = __shfl_xor(a[j], 32); ob[j] = __shfl_xor(b[j], 32); }
;                             if (fq < 2) { a = a * c0 - oa * s0; b = b * c1 - ob * s1; } else { a = a * c0 + oa * s0; b = b * c1 + ob * s1; }
;                             acc[ai][bj][m][0] = a; acc[ai][bj][m][1] = b;
;                         }
;                     }
	v_pk_mul_f32 v[138:139], v[138:139], v[180:181]
	v_pk_mul_f32 v[136:137], v[136:137], v[176:177]
	v_pk_mul_f32 v[130:131], v[78:79], v[130:131]
	v_pk_mul_f32 v[128:129], v[76:77], v[128:129]
	s_waitcnt lgkmcnt(0)
	v_pk_mul_f32 v[134:135], v[134:135], v[182:183]
	v_pk_mul_f32 v[132:133], v[132:133], v[178:179]
	s_and_saveexec_b64 s[14:15], s[10:11]
	s_xor_b64 s[14:15], exec, s[14:15]
	v_pk_add_f32 v[62:63], v[142:143], v[138:139]
	v_pk_add_f32 v[60:61], v[140:141], v[136:137]
	v_pk_add_f32 v[78:79], v[130:131], v[134:135]
	v_pk_add_f32 v[76:77], v[128:129], v[132:133]
	s_andn2_saveexec_b64 s[14:15], s[14:15]
	v_sub_f32_e32 v63, v143, v139
	v_sub_f32_e32 v62, v142, v138
	v_sub_f32_e32 v61, v141, v137
	v_sub_f32_e32 v60, v140, v136
	v_sub_f32_e32 v79, v131, v135
	v_sub_f32_e32 v78, v130, v134
	v_sub_f32_e32 v77, v129, v133
	v_sub_f32_e32 v76, v128, v132
	s_or_b64 exec, exec, s[14:15]
	v_add_co_u32_e32 v132, vcc, 0x40000, v174
	global_load_dwordx4 v[128:131], v[174:175], off offset:3088
	global_load_dwordx4 v[140:143], v[174:175], off offset:3072
	v_addc_co_u32_e32 v133, vcc, 0, v175, vcc
	global_load_dwordx4 v[136:139], v[132:133], off offset:3072
	v_lshl_add_u64 v[132:133], v[174:175], 0, s[36:37]
	global_load_dwordx4 v[132:135], v[132:133], off offset:16
	ds_bpermute_b32 v182, v198, v0
	ds_bpermute_b32 v184, v198, v4
	ds_bpermute_b32 v183, v198, v1
	ds_bpermute_b32 v185, v198, v5
	ds_bpermute_b32 v188, v198, v2
	ds_bpermute_b32 v190, v198, v6
	ds_bpermute_b32 v189, v198, v3
	ds_bpermute_b32 v191, v198, v7
	s_waitcnt vmcnt(3)
	v_pk_mul_f32 v[178:179], v[6:7], v[130:131]
	s_waitcnt vmcnt(2)
	v_pk_mul_f32 v[174:175], v[2:3], v[142:143]
	v_pk_mul_f32 v[176:177], v[0:1], v[140:141]
	v_pk_mul_f32 v[180:181], v[4:5], v[128:129]
	s_waitcnt vmcnt(1) lgkmcnt(5)
	v_pk_mul_f32 v[186:187], v[136:137], v[182:183]
	s_waitcnt lgkmcnt(1)
	v_pk_mul_f32 v[188:189], v[138:139], v[188:189]
	s_waitcnt vmcnt(0) lgkmcnt(0)
	v_pk_mul_f32 v[182:183], v[134:135], v[190:191]
	v_pk_mul_f32 v[184:185], v[132:133], v[184:185]
	s_and_saveexec_b64 s[14:15], s[10:11]
	s_xor_b64 s[14:15], exec, s[14:15]
	v_pk_add_f32 v[2:3], v[174:175], v[188:189]
	v_pk_add_f32 v[0:1], v[176:177], v[186:187]
	v_pk_add_f32 v[6:7], v[178:179], v[182:183]
	v_pk_add_f32 v[4:5], v[180:181], v[184:185]
	s_andn2_saveexec_b64 s[14:15], s[14:15]
	v_sub_f32_e32 v3, v175, v189
	v_sub_f32_e32 v2, v174, v188
	v_sub_f32_e32 v1, v177, v187
	v_sub_f32_e32 v0, v176, v186
	v_sub_f32_e32 v7, v179, v183
	v_sub_f32_e32 v6, v178, v182
	v_sub_f32_e32 v5, v181, v185
	v_sub_f32_e32 v4, v180, v184
	s_or_b64 exec, exec, s[14:15]
	ds_bpermute_b32 v174, v198, v24
	ds_bpermute_b32 v176, v198, v44
	ds_bpermute_b32 v175, v198, v25
	ds_bpermute_b32 v177, v198, v45
	ds_bpermute_b32 v178, v198, v26
	ds_bpermute_b32 v179, v198, v27
	ds_bpermute_b32 v180, v198, v46
	ds_bpermute_b32 v181, v198, v47
	v_pk_mul_f32 v[142:143], v[26:27], v[142:143]
	v_pk_mul_f32 v[140:141], v[24:25], v[140:141]
	s_waitcnt lgkmcnt(2)
	v_pk_mul_f32 v[138:139], v[138:139], v[178:179]
	v_pk_mul_f32 v[136:137], v[136:137], v[174:175]
	v_pk_mul_f32 v[130:131], v[46:47], v[130:131]
	v_pk_mul_f32 v[128:129], v[44:45], v[128:129]
	s_waitcnt lgkmcnt(0)
	v_pk_mul_f32 v[134:135], v[134:135], v[180:181]
	v_pk_mul_f32 v[132:133], v[132:133], v[176:177]
	s_and_saveexec_b64 s[14:15], s[10:11]
	s_xor_b64 s[14:15], exec, s[14:15]
	v_pk_add_f32 v[26:27], v[142:143], v[138:139]
	v_pk_add_f32 v[24:25], v[140:141], v[136:137]
	v_pk_add_f32 v[46:47], v[130:131], v[134:135]
	v_pk_add_f32 v[44:45], v[128:129], v[132:133]
	s_andn2_saveexec_b64 s[14:15], s[14:15]
	v_sub_f32_e32 v27, v143, v139
	v_sub_f32_e32 v26, v142, v138
	v_sub_f32_e32 v25, v141, v137
	v_sub_f32_e32 v24, v140, v136
	v_sub_f32_e32 v47, v131, v135
	v_sub_f32_e32 v46, v130, v134
	v_sub_f32_e32 v45, v129, v133
	v_sub_f32_e32 v44, v128, v132
	s_or_b64 exec, exec, s[14:15]
